# LN1 panel-statistics exchange: agent-scope L1 invalidate issued before the poll loop instead of after it (5 sites); plus unit-end lgkmcnt-only wait
# speedup vs baseline: 1.0009x; 1.0009x over previous
.LBB0_601:
	s_or_b64 exec, exec, s[14:15]
	s_cmp_gt_u32 s21, 63
	s_cbranch_scc1 .LBB0_619
	buffer_inv sc1
	s_memrealtime s[14:15]
	s_lshl_b32 s22, s0, 6
	s_ashr_i32 s23, s22, 31
	s_lshl_b64 s[22:23], s[22:23], 2
	s_add_u32 s24, s38, s22
	s_addc_u32 s25, s39, s23
	v_mov_b32_e32 v133, 0
	v_mov_b64_e32 v[130:131], 0x1e8481
	s_branch .LBB0_605

.LBB0_615:
	s_waitcnt lgkmcnt(0)
	s_and_saveexec_b64 s[14:15], s[6:7]
	s_cbranch_execz .LBB0_618
	s_waitcnt vmcnt(0)
	s_and_b64 exec, exec, s[4:5]
	v_cndmask_b32_e64 v130, 0, 1, s[0:1]
	v_mov_b32_e32 v131, 0
	ds_write_b32 v131, v130 offset:10240

.LBB0_650:
	s_or_b64 exec, exec, s[14:15]
	s_cmp_gt_u32 s19, 63
	s_cbranch_scc1 .LBB0_668
	buffer_inv sc1
	s_memrealtime s[14:15]
	s_lshl_b32 s16, s0, 6
	s_ashr_i32 s17, s16, 31
	s_lshl_b64 s[16:17], s[16:17], 2
	s_add_u32 s16, s38, s16
	s_addc_u32 s17, s39, s17
	v_mov_b32_e32 v133, 0
	v_mov_b64_e32 v[130:131], 0x1e8481
	s_branch .LBB0_654

.LBB0_1525:
	s_or_b64 exec, exec, s[52:53]
	s_andn2_b64 vcc, exec, s[36:37]
	s_cbranch_vccnz .LBB0_1542
	buffer_inv sc1
	s_memrealtime s[52:53]
	s_lshl_b32 s54, s0, 6
	s_ashr_i32 s55, s54, 31
	s_lshl_b64 s[54:55], s[54:55], 2
	s_add_u32 s54, s94, s54
	s_addc_u32 s55, s95, s55
	s_branch .LBB0_1529

.LBB0_1539:
	s_waitcnt vmcnt(0)
	s_and_b64 exec, exec, s[4:5]
	v_cndmask_b32_e64 v3, 0, 1, s[0:1]
	v_mov_b32_e32 v4, s71
	ds_write_b32 v4, v3

.LBB0_2404:
	s_or_b64 exec, exec, s[46:47]
	s_andn2_b64 vcc, exec, s[28:29]
	s_cbranch_vccnz .LBB0_2421
	buffer_inv sc1
	s_memrealtime s[46:47]
	s_lshl_b32 s48, s0, 6
	s_ashr_i32 s49, s48, 31
	s_lshl_b64 s[48:49], s[48:49], 2
	s_add_u32 s48, s65, s48
	s_addc_u32 s49, s66, s49
	s_branch .LBB0_2408

.LBB0_2418:
	s_waitcnt vmcnt(0)
	s_and_b64 exec, exec, s[4:5]
	v_cndmask_b32_e64 v3, 0, 1, s[0:1]
	v_mov_b32_e32 v4, s81
	ds_write_b32 v4, v3
